# attention key loop: next tile's K/V loads and the QK accumulator init moved from the head of the compute segment to before the second barrier (behind the K/V ds_writes); on top of the static priority
# baseline (speedup 1.0000x reference)
.LBB0_270:
	s_add_i32 s12, s40, 1
	s_cmp_ge_u32 s12, s21
	s_waitcnt lgkmcnt(0)
	s_barrier
	s_waitcnt vmcnt(7)
	ds_write_b128 v250, v[176:179]
	s_waitcnt vmcnt(6)
	ds_write_b128 v250, v[180:183] offset:16384
	s_waitcnt vmcnt(5)
	ds_write_b128 v250, v[184:187] offset:8192
	s_waitcnt vmcnt(4)
	ds_write_b128 v250, v[188:191] offset:24576
	s_waitcnt vmcnt(1)
	ds_write_b128 v251, v[196:199]
	ds_write_b128 v251, v[192:195] offset:4096
	ds_write_b128 v251, v[200:203] offset:8192
	s_waitcnt vmcnt(0)
	ds_write_b128 v251, v[204:207] offset:12288
	s_cbranch_scc1 .Lattn_skipld
	s_mul_i32 s10, s18, 0x4800
	s_mul_hi_u32 s11, s18, 0x4800
	s_add_u32 s10, s8, s10
	s_addc_u32 s11, s9, s11
	v_lshl_add_u64 v[2:3], s[10:11], 0, v[214:215]
	global_load_dwordx4 v[176:179], v[2:3], off
	global_load_dwordx4 v[180:183], v[2:3], off offset:256
	v_add_co_u32_e32 v2, vcc, 0x90000, v2
	s_nop 1
	v_addc_co_u32_e32 v3, vcc, 0, v3, vcc
	global_load_dwordx4 v[184:187], v[2:3], off
	global_load_dwordx4 v[188:191], v[2:3], off offset:256
	v_lshl_add_u64 v[2:3], s[10:11], 0, v[216:217]
	v_add_co_u32_e32 v4, vcc, 0x48000, v2
	s_nop 1
	v_addc_co_u32_e32 v5, vcc, 0, v3, vcc
	global_load_dwordx4 v[196:199], v[2:3], off
	global_load_dwordx4 v[192:195], v[4:5], off
	v_add_co_u32_e32 v4, vcc, 0x90000, v2
	s_nop 1
	v_addc_co_u32_e32 v5, vcc, 0, v3, vcc
	v_add_co_u32_e32 v2, vcc, 0xd8000, v2
	s_nop 1
	v_addc_co_u32_e32 v3, vcc, 0, v3, vcc
	global_load_dwordx4 v[200:203], v[4:5], off
	global_load_dwordx4 v[204:207], v[2:3], off
.Lattn_skipld:
	v_cvt_f32_i32_e32 v0, v249
	s_cmp_eq_u32 s40, 0
	s_cselect_b64 s[10:11], -1, 0
	v_cndmask_b32_e64 v2, v208, 0, s[10:11]
	s_mov_b32 s4, 0x41200000
	v_fma_f32 v0, v218, v0, -v2
	s_mov_b32 s5, 0x41300000
	v_pk_fma_f32 v[150:151], v[220:221], s[4:5], v[0:1] op_sel_hi:[1,1,0]
	s_mov_b32 s4, 0x41900000
	s_mov_b32 s5, 0x41980000
	v_pk_fma_f32 v[154:155], v[220:221], s[4:5], v[0:1] op_sel_hi:[1,1,0]
	s_mov_b32 s4, 0x41c00000
	s_mov_b32 s5, 0x41c80000
	v_pk_fma_f32 v[156:157], v[220:221], s[4:5], v[0:1] op_sel_hi:[1,1,0]
	s_mov_b32 s4, 0x41d00000
	s_mov_b32 s5, 0x41d80000
	v_pk_fma_f32 v[158:159], v[220:221], s[4:5], v[0:1] op_sel_hi:[1,1,0]
	s_mov_b32 s4, 0x42680000
	v_mov_b32_e32 v219, v218
	s_mov_b32 s5, 0x426c0000
	v_pk_fma_f32 v[174:175], v[218:219], s[4:5], v[0:1] op_sel_hi:[1,1,0]
	s_mov_b32 s4, 0x42600000
	s_mov_b32 s5, 0x42640000
	v_pk_fma_f32 v[172:173], v[218:219], s[4:5], v[0:1] op_sel_hi:[1,1,0]
	s_mov_b32 s4, 0x42480000
	s_mov_b32 s5, 0x424c0000
	v_pk_fma_f32 v[170:171], v[218:219], s[4:5], v[0:1] op_sel_hi:[1,1,0]
	s_mov_b32 s4, 0x42400000
	s_mov_b32 s5, 0x42440000
	v_pk_fma_f32 v[168:169], v[218:219], s[4:5], v[0:1] op_sel_hi:[1,1,0]
	s_mov_b32 s4, 0x42280000
	s_mov_b32 s5, 0x422c0000
	v_pk_fma_f32 v[166:167], v[218:219], s[4:5], v[0:1] op_sel_hi:[1,1,0]
	s_mov_b32 s4, 0x42200000
	s_mov_b32 s5, 0x42240000
	v_pk_fma_f32 v[164:165], v[218:219], s[4:5], v[0:1] op_sel_hi:[1,1,0]
	s_mov_b32 s4, 0x42080000
	s_mov_b32 s5, 0x420c0000
	v_pk_fma_f32 v[162:163], v[218:219], s[4:5], v[0:1] op_sel_hi:[1,1,0]
	s_mov_b32 s4, 0x42000000
	s_mov_b32 s5, 0x42040000
	v_fma_f32 v144, 0, v218, v0
	v_add_f32_e32 v145, v218, v0
	v_pk_fma_f32 v[146:147], v[220:221], s[28:29], v[0:1] op_sel_hi:[1,1,0]
	v_pk_fma_f32 v[148:149], v[220:221], s[96:97], v[0:1] op_sel_hi:[1,1,0]
	v_pk_fma_f32 v[152:153], v[220:221], s[2:3], v[0:1] op_sel_hi:[1,1,0]
	v_pk_fma_f32 v[160:161], v[222:223], s[4:5], v[0:1] op_sel_hi:[1,1,0]
	s_waitcnt lgkmcnt(0)
	s_barrier
.LBB0_272:
	v_add_u32_e32 v10, s23, v241
	ds_read_b128 v[2:5], v10
	v_add_u32_e32 v6, s17, v241
	ds_read_b128 v[6:9], v6
	ds_read_b128 v[10:13], v10 offset:8192
	v_add_u32_e32 v0, s23, v242
	s_waitcnt lgkmcnt(1)
	v_mfma_f32_32x32x16_bf16 v[144:159], v[2:5], v[6:9], v[144:159]
	ds_read_b128 v[2:5], v0
	s_cmp_lt_u32 s40, s70
	s_waitcnt lgkmcnt(1)
	v_mfma_f32_32x32x16_bf16 v[160:175], v[10:13], v[6:9], v[160:175]
	v_add_u32_e32 v6, s17, v242
	ds_read_b128 v[6:9], v6
	s_waitcnt lgkmcnt(0)
	v_mfma_f32_32x32x16_bf16 v[144:159], v[2:5], v[6:9], v[144:159]
	ds_read_b128 v[2:5], v0 offset:8192
	v_add_u32_e32 v0, s23, v243
	s_waitcnt lgkmcnt(0)
	v_mfma_f32_32x32x16_bf16 v[160:175], v[2:5], v[6:9], v[160:175]
	ds_read_b128 v[2:5], v0
	v_add_u32_e32 v6, s17, v243
	ds_read_b128 v[6:9], v6
	s_waitcnt lgkmcnt(0)
	v_mfma_f32_32x32x16_bf16 v[144:159], v[2:5], v[6:9], v[144:159]
	ds_read_b128 v[2:5], v0 offset:8192
	v_add_u32_e32 v0, s23, v244
	s_waitcnt lgkmcnt(0)
	v_mfma_f32_32x32x16_bf16 v[160:175], v[2:5], v[6:9], v[160:175]
	ds_read_b128 v[2:5], v0
	v_add_u32_e32 v6, s17, v244
	ds_read_b128 v[6:9], v6
	s_waitcnt lgkmcnt(0)
	v_mfma_f32_32x32x16_bf16 v[144:159], v[2:5], v[6:9], v[144:159]
	ds_read_b128 v[2:5], v0 offset:8192
	v_add_u32_e32 v0, s23, v245
	s_waitcnt lgkmcnt(0)
	v_mfma_f32_32x32x16_bf16 v[160:175], v[2:5], v[6:9], v[160:175]
	ds_read_b128 v[2:5], v0
	v_add_u32_e32 v6, s17, v245
	ds_read_b128 v[6:9], v6
	s_waitcnt lgkmcnt(0)
	v_mfma_f32_32x32x16_bf16 v[144:159], v[2:5], v[6:9], v[144:159]
	ds_read_b128 v[2:5], v0 offset:8192
	v_add_u32_e32 v0, s23, v246
	s_waitcnt lgkmcnt(0)
	v_mfma_f32_32x32x16_bf16 v[160:175], v[2:5], v[6:9], v[160:175]
	ds_read_b128 v[2:5], v0
	v_add_u32_e32 v6, s17, v246
	ds_read_b128 v[6:9], v6
	s_waitcnt lgkmcnt(0)
	v_mfma_f32_32x32x16_bf16 v[144:159], v[2:5], v[6:9], v[144:159]
	ds_read_b128 v[2:5], v0 offset:8192
	v_add_u32_e32 v0, s23, v247
	s_waitcnt lgkmcnt(0)
	v_mfma_f32_32x32x16_bf16 v[160:175], v[2:5], v[6:9], v[160:175]
	ds_read_b128 v[2:5], v0
	v_add_u32_e32 v6, s17, v247
	ds_read_b128 v[6:9], v6
	s_waitcnt lgkmcnt(0)
	v_mfma_f32_32x32x16_bf16 v[144:159], v[2:5], v[6:9], v[144:159]
	ds_read_b128 v[2:5], v0 offset:8192
	v_add_u32_e32 v0, s23, v248
	s_waitcnt lgkmcnt(0)
	v_mfma_f32_32x32x16_bf16 v[160:175], v[2:5], v[6:9], v[160:175]
	ds_read_b128 v[2:5], v0
	v_add_u32_e32 v6, s17, v248
	ds_read_b128 v[6:9], v6
	s_waitcnt lgkmcnt(0)
	v_mfma_f32_32x32x16_bf16 v[144:159], v[2:5], v[6:9], v[144:159]
	ds_read_b128 v[2:5], v0 offset:8192
	s_waitcnt lgkmcnt(0)
	v_mfma_f32_32x32x16_bf16 v[160:175], v[2:5], v[6:9], v[160:175]
	s_cbranch_scc1 .LBB0_274
	s_movk_i32 s66, 0xffe6
	s_movk_i32 s96, 0xffe5
	s_movk_i32 s64, 0xffe7
	s_mov_b64 s[28:29], s[94:95]
	v_cmp_lt_i32_e64 s[94:95], s66, v249
	v_cmp_lt_i32_e64 s[96:97], s96, v249
	s_movk_i32 s4, 0xffe0
	s_movk_i32 s62, 0xffe8
	s_mov_b64 s[6:7], s[92:93]
	v_cmp_lt_i32_e64 s[92:93], s64, v249
	s_and_b64 s[94:95], s[96:97], s[94:95]
	v_cmp_lt_i32_e32 vcc, s4, v249
	s_movk_i32 s60, 0xffed
	s_mov_b64 s[4:5], s[90:91]
	v_cmp_lt_i32_e64 s[90:91], s62, v249
	s_and_b64 s[92:93], s[94:95], s[92:93]
	s_movk_i32 s58, 0xffee
	v_cmp_lt_i32_e64 s[88:89], s60, v249
	s_and_b64 s[90:91], s[92:93], s[90:91]
	s_movk_i32 s56, 0xffef
	v_cmp_lt_i32_e64 s[86:87], s58, v249
	s_and_b64 s[88:89], s[90:91], s[88:89]
	v_cmp_lt_i32_e64 s[84:85], s56, v249
	s_and_b64 s[86:87], s[88:89], s[86:87]
	v_cmp_lt_i32_e64 s[82:83], -16, v249
	s_and_b64 s[84:85], s[86:87], s[84:85]
	v_cmp_lt_i32_e64 s[80:81], -11, v249
	s_and_b64 s[82:83], s[84:85], s[82:83]
	v_cmp_lt_i32_e64 s[78:79], -10, v249
	s_and_b64 s[80:81], s[82:83], s[80:81]
	v_cmp_lt_i32_e64 s[76:77], -9, v249
	s_and_b64 s[78:79], s[80:81], s[78:79]
	s_mov_b32 s0, s74
	v_cmp_lt_i32_e64 s[74:75], -8, v249
	s_and_b64 s[76:77], s[78:79], s[76:77]
	v_cmp_gt_i32_e64 s[40:41], 1, v249
	v_cmp_gt_i32_e64 s[42:43], 0, v249
	v_cmp_lt_i32_e64 s[72:73], -3, v249
	s_and_b64 s[74:75], s[76:77], s[74:75]
	s_or_b64 s[40:41], s[42:43], s[40:41]
	v_cmp_lt_i32_e64 s[68:69], -2, v249
	s_and_b64 s[72:73], s[74:75], s[72:73]
	v_cndmask_b32_e64 v0, v234, v145, s[42:43]
	v_cndmask_b32_e64 v2, v234, v144, s[40:41]
	s_and_b64 s[68:69], s[72:73], s[68:69]
	s_movk_i32 s66, 0xffc6
	v_cndmask_b32_e64 v144, v144, v2, s[68:69]
	v_cndmask_b32_e64 v146, v146, v234, s[68:69]
	v_cndmask_b32_e64 v145, v145, v0, s[68:69]
	s_movk_i32 s68, 0xffc5
	s_movk_i32 s64, 0xffc7
	v_cmp_lt_i32_e64 s[66:67], s66, v249
	v_cmp_lt_i32_e64 s[68:69], s68, v249
	s_movk_i32 s62, 0xffc8
	v_cmp_lt_i32_e64 s[64:65], s64, v249
	s_and_b64 s[66:67], s[68:69], s[66:67]
	s_movk_i32 s60, 0xffcd
	v_cmp_lt_i32_e64 s[62:63], s62, v249
	s_and_b64 s[64:65], s[66:67], s[64:65]
	s_movk_i32 s58, 0xffce
	v_cmp_lt_i32_e64 s[60:61], s60, v249
	s_and_b64 s[62:63], s[64:65], s[62:63]
	s_movk_i32 s56, 0xffcf
	v_cmp_lt_i32_e64 s[58:59], s58, v249
	s_and_b64 s[60:61], s[62:63], s[60:61]
	s_movk_i32 s54, 0xffd0
	v_cmp_lt_i32_e64 s[56:57], s56, v249
	s_and_b64 s[58:59], s[60:61], s[58:59]
	s_movk_i32 s52, 0xffd5
	v_cmp_lt_i32_e64 s[54:55], s54, v249
	s_and_b64 s[56:57], s[58:59], s[56:57]
	s_movk_i32 s50, 0xffd6
	v_cmp_lt_i32_e64 s[52:53], s52, v249
	s_and_b64 s[54:55], s[56:57], s[54:55]
	s_movk_i32 s48, 0xffd7
	v_cmp_lt_i32_e64 s[50:51], s50, v249
	s_and_b64 s[52:53], s[54:55], s[52:53]
	s_movk_i32 s46, 0xffd8
	v_cmp_lt_i32_e64 s[48:49], s48, v249
	s_and_b64 s[50:51], s[52:53], s[50:51]
	s_movk_i32 s44, 0xffdd
	v_cmp_lt_i32_e64 s[46:47], s46, v249
	s_and_b64 s[48:49], s[50:51], s[48:49]
	s_movk_i32 s42, 0xffde
	v_cmp_lt_i32_e64 s[44:45], s44, v249
	s_and_b64 s[46:47], s[48:49], s[46:47]
	s_movk_i32 s40, 0xffdf
	v_cmp_lt_i32_e64 s[42:43], s42, v249
	s_and_b64 s[44:45], s[46:47], s[44:45]
	v_cmp_lt_i32_e64 s[40:41], s40, v249
	s_and_b64 s[42:43], s[44:45], s[42:43]
	s_and_b64 s[40:41], s[42:43], s[40:41]
	v_cndmask_b32_e64 v159, v159, v234, s[96:97]
	s_mov_b32 s96, 0x41000000
	v_cndmask_b32_e64 v158, v158, v234, s[94:95]
	s_mov_b64 s[94:95], s[28:29]
	s_mov_b32 s28, 2.0
	s_and_b64 vcc, s[40:41], vcc
	s_mov_b32 s97, 0x41100000
	s_mov_b32 s29, 0x40400000
	v_cndmask_b32_e64 v157, v157, v234, s[92:93]
	s_mov_b64 s[92:93], s[6:7]
	v_cndmask_b32_e64 v156, v156, v234, s[90:91]
	s_mov_b64 s[90:91], s[4:5]
	v_cndmask_b32_e64 v155, v155, v234, s[88:89]
	s_movk_i32 s89, 0xfe3f
	v_cndmask_b32_e64 v154, v154, v234, s[86:87]
	s_mov_b64 s[86:87], 0x800
	v_cndmask_b32_e64 v153, v153, v234, s[84:85]
	v_cndmask_b32_e64 v152, v152, v234, s[82:83]
	v_cndmask_b32_e64 v151, v151, v234, s[80:81]
	v_cndmask_b32_e64 v150, v150, v234, s[78:79]
	v_cndmask_b32_e64 v149, v149, v234, s[76:77]
	v_cndmask_b32_e64 v148, v148, v234, s[74:75]
	s_mov_b32 s74, s0
	s_mov_b64 s[0:1], 0x1000
	v_cndmask_b32_e64 v147, v147, v234, s[72:73]
	v_cndmask_b32_e64 v175, v175, v234, s[68:69]
	v_cndmask_b32_e64 v174, v174, v234, s[66:67]
	v_cndmask_b32_e64 v173, v173, v234, s[64:65]
	v_cndmask_b32_e64 v172, v172, v234, s[62:63]
	v_cndmask_b32_e64 v171, v171, v234, s[60:61]
	v_cndmask_b32_e64 v170, v170, v234, s[58:59]
	v_cndmask_b32_e64 v169, v169, v234, s[56:57]
	v_cndmask_b32_e64 v168, v168, v234, s[54:55]
	v_cndmask_b32_e64 v167, v167, v234, s[52:53]
	v_cndmask_b32_e64 v166, v166, v234, s[50:51]
	v_cndmask_b32_e64 v165, v165, v234, s[48:49]
	v_cndmask_b32_e64 v164, v164, v234, s[46:47]
	v_cndmask_b32_e64 v163, v163, v234, s[44:45]
	v_cndmask_b32_e64 v162, v162, v234, s[42:43]
	v_cndmask_b32_e64 v161, v161, v234, s[40:41]
	v_cndmask_b32_e32 v160, v160, v234, vcc
